# speedup vs baseline: 1.0132x; 1.0086x over previous
_Z9k_redprepILi1EEvPKfPKjS1_S1_S1_S1_S1_PfPKDv8_DF16_S7_S1_PDF16_S4_S4_S4_PKiS7_S1_S1_S1_S4_S4_:
	s_load_dwordx8 s[4:11], s[0:1], 0x8
	v_readfirstlane_b32 s3, v0
	s_lshr_b32 s3, s3, 6
	s_cmp_ge_u32 s3, 4
	s_cbranch_scc0 .Lmy_prio1_done
	s_setprio 1
.Lmy_prio1_done:
	s_mov_b32 s12, s2
	s_lshl_b32 s92, s2, 5
	s_lshl_b32 s2, s3, 2
	v_and_b32_e32 v1, 63, v0
	s_add_i32 s16, s2, s92
	v_mov_b32_e32 v3, 0
	v_lshlrev_b32_e32 v2, 3, v1
	s_waitcnt lgkmcnt(0)
	s_cmp_eq_u64 s[10:11], 0
	v_writelane_b32 v102, s12, 0
	v_lshl_add_u64 v[4:5], s[4:5], 0, v[2:3]
	s_cselect_b64 s[4:5], -1, 0
	s_cmp_lg_u64 s[10:11], 0
	v_writelane_b32 v102, s13, 1
	s_cselect_b64 s[12:13], -1, 0
	s_ashr_i32 s17, s16, 31
	s_lshl_b64 s[14:15], s[16:17], 9
	v_writelane_b32 v102, s3, 2
	v_lshl_add_u64 v[6:7], v[4:5], 0, s[14:15]
	s_mov_b32 s3, 0x400000
	v_add_co_u32_e32 v8, vcc, s3, v6
	s_mov_b32 s3, 0x800000
	s_nop 0
	v_addc_co_u32_e32 v9, vcc, 0, v7, vcc
	v_add_co_u32_e32 v10, vcc, s3, v6
	s_mov_b32 s3, 0xc00000
	s_nop 0
	v_addc_co_u32_e32 v11, vcc, 0, v7, vcc
	v_add_co_u32_e32 v12, vcc, s3, v6
	s_mov_b32 s3, 0x1000000
	s_nop 0
	v_addc_co_u32_e32 v13, vcc, 0, v7, vcc
	global_load_dwordx2 v[62:63], v[6:7], off
	global_load_dwordx2 v[66:67], v[8:9], off
	global_load_dwordx2 v[54:55], v[10:11], off
	global_load_dwordx2 v[58:59], v[12:13], off
	v_add_co_u32_e32 v8, vcc, s3, v6
	s_mov_b32 s3, 0x1400000
	s_nop 0
	v_addc_co_u32_e32 v9, vcc, 0, v7, vcc
	v_add_co_u32_e32 v10, vcc, s3, v6
	s_mov_b32 s3, 0x1800000
	s_nop 0
	v_addc_co_u32_e32 v11, vcc, 0, v7, vcc
	v_add_co_u32_e32 v12, vcc, s3, v6
	s_mov_b32 s3, 0x1c00000
	s_nop 0
	v_addc_co_u32_e32 v13, vcc, 0, v7, vcc
	v_add_co_u32_e32 v6, vcc, s3, v6
	s_lshl_b64 s[34:35], s[16:17], 2
	s_nop 0
	v_addc_co_u32_e32 v7, vcc, 0, v7, vcc
	global_load_dwordx2 v[60:61], v[8:9], off
	global_load_dwordx2 v[64:65], v[10:11], off
	global_load_dwordx2 v[52:53], v[12:13], off
	global_load_dwordx2 v[56:57], v[6:7], off
	s_add_u32 s44, s8, s34
	s_addc_u32 s45, s9, s35
	s_add_u32 s38, s6, s34
	s_addc_u32 s39, s7, s35
	s_add_u32 s40, s44, 0x8000
	s_addc_u32 s41, s45, 0
	s_add_u32 s42, s38, 0x8000
	s_addc_u32 s43, s39, 0
	s_add_u32 s46, s44, 0x10000
	s_addc_u32 s47, s45, 0
	s_add_u32 s54, s38, 0x10000
	s_addc_u32 s55, s39, 0
	s_add_u32 s56, s44, 0x18000
	s_addc_u32 s57, s45, 0
	s_add_u32 s60, s38, 0x18000
	s_addc_u32 s61, s39, 0
	s_add_u32 s62, s44, 0x20000
	s_addc_u32 s63, s45, 0
	s_add_u32 s64, s38, 0x20000
	s_addc_u32 s65, s39, 0
	s_add_u32 s68, s44, 0x28000
	s_addc_u32 s69, s45, 0
	s_add_u32 s70, s38, 0x28000
	s_addc_u32 s71, s39, 0
	s_add_u32 s74, s44, 0x30000
	s_addc_u32 s75, s45, 0
	s_add_u32 s76, s38, 0x30000
	s_addc_u32 s77, s39, 0
	v_bfe_u32 v2, v0, 1, 5
	v_lshlrev_b32_e32 v6, 7, v0
	s_movk_i32 s3, 0x80
	s_add_u32 s78, s44, 0x38000
	v_and_or_b32 v2, v6, s3, v2
	s_addc_u32 s79, s45, 0
	v_lshlrev_b32_e32 v2, 2, v2
	s_add_u32 s80, s38, 0x38000
	v_lshl_add_u64 v[68:69], s[10:11], 0, v[2:3]
	s_addc_u32 s81, s39, 0
	s_and_b64 vcc, exec, s[4:5]
	v_writelane_b32 v102, s2, 3
	s_cbranch_vccnz .LBB3_2
	s_lshl_b64 s[6:7], s[16:17], 10
	v_lshl_add_u64 v[6:7], v[68:69], 0, s[6:7]
	global_load_dword v84, v[6:7], off
	global_load_dword v83, v[6:7], off offset:128
	global_load_dword v78, v[6:7], off offset:256
	global_load_dword v74, v[6:7], off offset:384

.LBB4_2:
	s_or_b64 exec, exec, s[4:5]
	s_lshr_b32 s3, s84, 6
	s_cmp_ge_u32 s3, 4
	s_cbranch_scc0 .Lmy_prio2_done
	s_setprio 1
.Lmy_prio2_done:
	s_lshl_b32 s4, s3, 2
	s_add_i32 s22, s4, s33
	v_and_b32_e32 v1, 63, v0
	s_waitcnt lgkmcnt(0)
	s_cmp_eq_u64 s[14:15], 0
	v_mov_b32_e32 v3, 0
	v_lshlrev_b32_e32 v2, 3, v1
	s_cselect_b64 s[6:7], -1, 0
	s_cmp_lg_u64 s[14:15], 0
	v_lshl_add_u64 v[4:5], s[8:9], 0, v[2:3]
	s_cselect_b64 s[8:9], -1, 0
	s_ashr_i32 s23, s22, 31
	s_lshl_b64 s[4:5], s[22:23], 9
	v_lshl_add_u64 v[6:7], v[4:5], 0, s[4:5]
	s_mov_b32 s4, 0x400000
	v_add_co_u32_e32 v8, vcc, s4, v6
	s_mov_b32 s4, 0x800000
	s_nop 0
	v_addc_co_u32_e32 v9, vcc, 0, v7, vcc
	v_add_co_u32_e32 v10, vcc, s4, v6
	s_mov_b32 s4, 0xc00000
	s_nop 0
	v_addc_co_u32_e32 v11, vcc, 0, v7, vcc
	v_add_co_u32_e32 v12, vcc, s4, v6
	s_mov_b32 s4, 0x1000000
	s_nop 0
	v_addc_co_u32_e32 v13, vcc, 0, v7, vcc
	global_load_dwordx2 v[64:65], v[6:7], off
	global_load_dwordx2 v[66:67], v[8:9], off
	global_load_dwordx2 v[56:57], v[10:11], off
	global_load_dwordx2 v[58:59], v[12:13], off
	v_add_co_u32_e32 v8, vcc, s4, v6
	s_mov_b32 s4, 0x1400000
	s_nop 0
	v_addc_co_u32_e32 v9, vcc, 0, v7, vcc
	v_add_co_u32_e32 v10, vcc, s4, v6
	s_mov_b32 s4, 0x1800000
	s_nop 0
	v_addc_co_u32_e32 v11, vcc, 0, v7, vcc
	v_add_co_u32_e32 v12, vcc, s4, v6
	s_mov_b32 s4, 0x1c00000
	s_nop 0
	v_addc_co_u32_e32 v13, vcc, 0, v7, vcc
	v_add_co_u32_e32 v6, vcc, s4, v6
	v_bfe_u32 v2, v0, 1, 5
	s_nop 0
	v_addc_co_u32_e32 v7, vcc, 0, v7, vcc
	global_load_dwordx2 v[60:61], v[8:9], off
	global_load_dwordx2 v[62:63], v[10:11], off
	global_load_dwordx2 v[52:53], v[12:13], off
	global_load_dwordx2 v[54:55], v[6:7], off
	v_lshlrev_b32_e32 v6, 7, v0
	s_movk_i32 s4, 0x80
	v_and_or_b32 v2, v6, s4, v2
	s_lshl_b64 s[4:5], s[22:23], 2
	s_add_u32 s30, s12, s4
	s_addc_u32 s31, s13, s5
	s_add_u32 s24, s10, s4
	s_addc_u32 s25, s11, s5
	s_add_u32 s26, s30, 0x8000
	s_addc_u32 s27, s31, 0
	s_add_u32 s28, s24, 0x8000
	s_addc_u32 s29, s25, 0
	s_add_u32 s34, s30, 0x10000
	s_addc_u32 s35, s31, 0
	s_add_u32 s36, s24, 0x10000
	s_addc_u32 s37, s25, 0
	s_add_u32 s38, s30, 0x18000
	s_addc_u32 s39, s31, 0
	s_add_u32 s40, s24, 0x18000
	s_addc_u32 s41, s25, 0
	s_add_u32 s42, s30, 0x20000
	s_addc_u32 s43, s31, 0
	s_add_u32 s44, s24, 0x20000
	s_addc_u32 s45, s25, 0
	s_add_u32 s62, s30, 0x28000
	s_addc_u32 s63, s31, 0
	s_add_u32 s64, s24, 0x28000
	s_addc_u32 s65, s25, 0
	s_add_u32 s66, s30, 0x30000
	s_addc_u32 s67, s31, 0
	s_add_u32 s68, s24, 0x30000
	s_addc_u32 s69, s25, 0
	s_add_u32 s70, s30, 0x38000
	s_addc_u32 s71, s31, 0
	v_lshlrev_b32_e32 v2, 2, v2
	s_add_u32 s72, s24, 0x38000
	v_lshl_add_u64 v[68:69], s[14:15], 0, v[2:3]
	s_addc_u32 s73, s25, 0
	s_and_b64 vcc, exec, s[6:7]
	s_cbranch_vccnz .LBB4_4
	s_lshl_b64 s[4:5], s[22:23], 10
	v_lshl_add_u64 v[6:7], v[68:69], 0, s[4:5]
	global_load_dword v84, v[6:7], off
	global_load_dword v83, v[6:7], off offset:128
	global_load_dword v82, v[6:7], off offset:256
	global_load_dword v74, v[6:7], off offset:384
